# tail-aware stagger, 16 groups x 0.75us (index wg>>4)
# speedup vs baseline: 1.0030x; 1.0030x over previous
.LBB0_1847:
	s_or_b64 exec, exec, s[0:1]
	v_readlane_b32 s0, v254, 4
	s_mov_b32 s2, 0
	s_mov_b32 s4, s0
	v_readlane_b32 s54, v254, 2
	v_readlane_b32 s0, v254, 3
	s_waitcnt lgkmcnt(0)
	s_barrier
	s_lshr_b32 s98, s4, 4
	s_and_b32 s98, s98, 15
	s_cmp_eq_u32 s98, 0
	s_cbranch_scc1 .Lstg_done
.Lstg_loop:
	s_sleep 28
	s_add_i32 s98, s98, -1
	s_cmp_lg_u32 s98, 0
	s_cbranch_scc1 .Lstg_loop
.Lstg_done:
	v_readlane_b32 s100, v254, 26
	v_and_b32_e32 v251, 63, v0
	s_nop 1
	v_lshl_add_u32 v251, v251, 2, s100
	ds_read_b32 v251, v251
	s_mov_b32 s0, 23
	s_ashr_i32 s1, s0, 31
	s_lshl_b64 s[0:1], s[0:1], 3
	s_add_u32 s0, s94, s0
	s_addc_u32 s1, s95, s1
	s_load_dwordx2 s[24:25], s[0:1], 0x0
	v_readlane_b32 s0, v254, 50
	v_mov_b32_e32 v5, v0
	s_ashr_i32 s5, s4, 31
	v_mov_b32_e32 v2, s0
	ds_read_b32 v2, v2
	s_mov_b32 s55, 0
	v_readfirstlane_b32 s26, v5
	s_mov_b32 s3, 8
	s_mov_b64 s[0:1], s[4:5]
	s_waitcnt lgkmcnt(0)
	v_readfirstlane_b32 s6, v2
	s_ashr_i32 s7, s6, 31
	s_lshl_b64 s[10:11], s[6:7], 3
	v_mov_b64_e32 v[6:7], s[10:11]
	v_cmp_ge_i64_e32 vcc, s[4:5], v[6:7]
	v_cmp_lt_i64_e64 s[8:9], s[4:5], v[6:7]
	s_cbranch_vccz .LBB0_1849
	s_sub_u32 s0, s4, s10
	s_subb_u32 s1, s5, s11
	s_lshl_b64 s[6:7], s[6:7], 2
	v_mov_b64_e32 v[6:7], s[6:7]
	v_cmp_lt_i64_e64 s[8:9], s[0:1], v[6:7]
	s_mov_b32 s3, 4
	s_mov_b32 s55, 1
